# attention main loop: first four P.V MFMAs of each step issued inside the row-max section
# baseline (speedup 1.0000x reference)
.LBB0_1028:
	v_add_u32_e32 v230, s44, v243
	ds_read_b64_tr_b16 v[190:191], v230 offset:49152
	ds_read_b64_tr_b16 v[192:193], v230 offset:49664
	s_waitcnt lgkmcnt(9)
	v_mfma_f32_32x32x16_bf16 v[114:129], v[102:105], v[158:161], 0
	v_add_f32_e32 v106, v82, v83
	v_add_f32_e32 v106, v84, v106
	v_add_f32_e32 v106, v85, v106
	v_add_f32_e32 v106, v86, v106
	v_add_f32_e32 v106, v87, v106
	v_cvt_pk_bf16_f32 v150, v82, v83
	v_cvt_pk_bf16_f32 v151, v84, v85
	ds_read_b64_tr_b16 v[186:187], v230 offset:53248
	ds_read_b64_tr_b16 v[188:189], v230 offset:53760
	v_add_f32_e32 v82, v88, v106
	s_waitcnt lgkmcnt(10)
	v_mfma_f32_32x32x16_bf16 v[98:113], v[98:101], v[158:161], 0
	v_add_f32_e32 v82, v89, v82
	v_add_f32_e32 v82, v90, v82
	v_add_f32_e32 v130, v91, v82
	v_cvt_pk_bf16_f32 v152, v86, v87
	v_cvt_pk_bf16_f32 v153, v88, v89
	ds_read_b64_tr_b16 v[82:83], v230 offset:57344
	ds_read_b64_tr_b16 v[84:85], v230 offset:57856
	s_waitcnt lgkmcnt(11)
	v_mfma_f32_32x32x16_bf16 v[114:129], v[182:185], v[154:157], v[114:129]
	v_add_f32_e32 v86, v92, v130
	v_add_f32_e32 v86, v93, v86
	v_add_f32_e32 v86, v94, v86
	v_add_f32_e32 v130, v95, v86
	v_cvt_pk_bf16_f32 v138, v90, v91
	v_cvt_pk_bf16_f32 v139, v92, v93
	ds_read_b64_tr_b16 v[86:87], v230 offset:61440
	ds_read_b64_tr_b16 v[88:89], v230 offset:61952
	s_waitcnt lgkmcnt(12)
	v_mfma_f32_32x32x16_bf16 v[98:113], v[178:181], v[154:157], v[98:113]
	v_add_f32_e32 v90, v96, v130
	v_add_f32_e32 v90, v97, v90
	v_add_f32_e32 v90, v66, v90
	v_add_f32_e32 v130, v67, v90
	v_cvt_pk_bf16_f32 v140, v94, v95
	v_cvt_pk_bf16_f32 v141, v96, v97
	ds_read_b64_tr_b16 v[90:91], v230 offset:50176
	ds_read_b64_tr_b16 v[92:93], v230 offset:50688
	s_waitcnt lgkmcnt(13)
	v_mfma_f32_32x32x16_bf16 v[114:129], v[174:177], v[146:149], v[114:129]
	v_add_f32_e32 v94, v68, v130
	v_add_f32_e32 v94, v69, v94
	v_add_f32_e32 v94, v70, v94
	v_add_f32_e32 v130, v71, v94
	v_cvt_pk_bf16_f32 v134, v66, v67
	v_cvt_pk_bf16_f32 v135, v68, v69
	ds_read_b64_tr_b16 v[94:95], v230 offset:54272
	ds_read_b64_tr_b16 v[96:97], v230 offset:54784
	s_waitcnt lgkmcnt(14)
	v_mfma_f32_32x32x16_bf16 v[98:113], v[170:173], v[146:149], v[98:113]
	v_add_f32_e32 v66, v72, v130
	v_add_f32_e32 v66, v73, v66
	v_add_f32_e32 v66, v74, v66
	v_add_f32_e32 v66, v75, v66
	v_cvt_pk_bf16_f32 v136, v70, v71
	v_cvt_pk_bf16_f32 v137, v72, v73
	ds_read_b64_tr_b16 v[194:195], v230 offset:58368
	ds_read_b64_tr_b16 v[196:197], v230 offset:58880
	s_waitcnt lgkmcnt(14)
	v_mfma_f32_32x32x16_bf16 v[114:129], v[166:169], v[142:145], v[114:129]
	v_add_f32_e32 v66, v76, v66
	v_add_f32_e32 v66, v77, v66
	v_add_f32_e32 v66, v78, v66
	v_add_f32_e32 v66, v79, v66
	v_cvt_pk_bf16_f32 v130, v74, v75
	v_cvt_pk_bf16_f32 v131, v76, v77
	ds_read_b64_tr_b16 v[74:75], v230 offset:62464
	ds_read_b64_tr_b16 v[76:77], v230 offset:62976
	v_mfma_f32_32x32x16_bf16 v[98:113], v[162:165], v[142:145], v[98:113]
	v_add_f32_e32 v66, v80, v66
	v_add_f32_e32 v66, v81, v66
	v_add_f32_e32 v66, 0, v66
	v_cvt_pk_bf16_f32 v132, v78, v79
	v_cvt_pk_bf16_f32 v133, v80, v81
	s_add_i32 s4, s10, s89
	s_mov_b32 s5, m0
	s_mov_b32 m0, s4
	s_nop 0
	global_load_lds_dwordx4 v[220:221], off
	s_mov_b32 m0, s5
	v_add_f32_e32 v234, v234, v66
	s_addk_i32 s4, 0x400
	s_mov_b32 s5, m0
	s_mov_b32 m0, s4
	s_nop 0
	global_load_lds_dwordx4 v[218:219], off
	s_mov_b32 m0, s5
	v_lshl_add_u64 v[66:67], v[224:225], 0, s[0:1]
	s_add_i32 s4, s9, s70
	s_mov_b32 s5, m0
	s_mov_b32 m0, s4
	s_nop 0
	global_load_lds_dwordx4 v[66:67], off
	s_mov_b32 m0, s5
	v_lshl_add_u64 v[66:67], v[224:225], 0, s[64:65]
	s_addk_i32 s4, 0x400
	s_mov_b32 s5, m0
	s_mov_b32 m0, s4
	s_nop 0
	global_load_lds_dwordx4 v[66:67], off
	s_mov_b32 m0, s5
	s_waitcnt lgkmcnt(14)
	v_mfma_f32_32x32x16_bf16 v[2:17], v[150:153], v[190:193], v[2:17]
	v_max_f32_e32 v66, v115, v115
	v_max_f32_e32 v67, v114, v114
	v_max_f32_e32 v66, v67, v66
	v_max3_f32 v67, v116, v117, v99
	v_max3_f32 v66, v66, v98, v100
	v_max3_f32 v66, v66, v101, v118
	v_max3_f32 v67, v67, v120, v121
	v_max3_f32 v66, v66, v119, v102
	v_max3_f32 v67, v67, v104, v105
	s_waitcnt lgkmcnt(12)
	v_mfma_f32_32x32x16_bf16 v[50:65], v[150:153], v[186:189], v[50:65]
	v_max3_f32 v66, v66, v103, v122
	v_max3_f32 v67, v67, v124, v125
	v_max3_f32 v66, v66, v123, v106
	v_max3_f32 v67, v67, v108, v109
	v_max3_f32 v66, v66, v107, v126
	v_max3_f32 v67, v67, v128, v129
	s_waitcnt lgkmcnt(10)
	v_mfma_f32_32x32x16_bf16 v[34:49], v[150:153], v[82:85], v[34:49]
	v_max3_f32 v66, v66, v127, v110
	v_max3_f32 v67, v67, v112, v113
	v_max3_f32 v66, v66, v111, v67
	v_mov_b32_e32 v67, v66
	s_waitcnt lgkmcnt(8)
	v_mfma_f32_32x32x16_bf16 v[18:33], v[150:153], v[86:89], v[18:33]
	v_permlane32_swap_b32_e32 v66, v67
	v_max_f32_e32 v67, v67, v67
	v_max_f32_e32 v66, v66, v66
	v_max_f32_e32 v66, v66, v67
	v_sub_f32_e32 v66, v66, v207
	v_cmp_lt_f32_e32 vcc, s3, v66
	s_cmp_lg_u64 vcc, 0
	s_cselect_b64 s[4:5], -1, 0
	s_cbranch_vccnz .LBB0_1036
.LBB0_1029:
	s_add_i32 s6, s9, 0
	v_add_u32_e32 v66, s6, v209
	ds_read_b128 v[70:73], v66
	ds_read_b128 v[66:69], v66 offset:8192
	v_sub_f32_e32 v78, v114, v207
	v_exp_f32_e32 v114, v78
	v_sub_f32_e32 v78, v115, v207
	v_exp_f32_e32 v115, v78
	v_add_u32_e32 v78, s6, v213
	ds_read_b128 v[182:185], v78
	ds_read_b128 v[178:181], v78 offset:8192
	v_sub_f32_e32 v78, v116, v207
	v_exp_f32_e32 v116, v78
	v_sub_f32_e32 v78, v117, v207
	v_exp_f32_e32 v117, v78
	v_add_u32_e32 v78, s6, v251
	ds_read_b128 v[174:177], v78
	ds_read_b128 v[170:173], v78 offset:8192
	v_sub_f32_e32 v78, v118, v207
	v_exp_f32_e32 v118, v78
	v_sub_f32_e32 v78, v119, v207
	v_exp_f32_e32 v119, v78
	v_add_u32_e32 v78, s6, v235
	ds_read_b128 v[166:169], v78
	ds_read_b128 v[162:165], v78 offset:8192
	v_sub_f32_e32 v78, v120, v207
	v_exp_f32_e32 v120, v78
	v_sub_f32_e32 v78, v121, v207
	v_exp_f32_e32 v121, v78
	ds_read_b64_tr_b16 v[78:79], v230 offset:51200
	ds_read_b64_tr_b16 v[80:81], v230 offset:51712
	s_waitcnt lgkmcnt(14)
	v_mfma_f32_32x32x16_bf16 v[2:17], v[138:141], v[90:93], v[2:17]
	v_sub_f32_e32 v82, v122, v207
	v_exp_f32_e32 v122, v82
	v_sub_f32_e32 v82, v123, v207
	v_exp_f32_e32 v123, v82
	ds_read_b64_tr_b16 v[82:83], v230 offset:55296
	ds_read_b64_tr_b16 v[84:85], v230 offset:55808
	v_mfma_f32_32x32x16_bf16 v[50:65], v[138:141], v[94:97], v[50:65]
	v_sub_f32_e32 v86, v124, v207
	v_exp_f32_e32 v124, v86
	v_sub_f32_e32 v86, v125, v207
	v_exp_f32_e32 v125, v86
	ds_read_b64_tr_b16 v[86:87], v230 offset:59392
	ds_read_b64_tr_b16 v[88:89], v230 offset:59904
	s_waitcnt lgkmcnt(14)
	v_mfma_f32_32x32x16_bf16 v[34:49], v[138:141], v[194:197], v[34:49]
	v_sub_f32_e32 v90, v126, v207
	v_exp_f32_e32 v126, v90
	v_sub_f32_e32 v90, v127, v207
	v_exp_f32_e32 v127, v90
	ds_read_b64_tr_b16 v[90:91], v230 offset:63488
	ds_read_b64_tr_b16 v[92:93], v230 offset:64000
	v_mfma_f32_32x32x16_bf16 v[18:33], v[138:141], v[74:77], v[18:33]
	v_sub_f32_e32 v74, v128, v207
	v_exp_f32_e32 v128, v74
	v_sub_f32_e32 v74, v129, v207
	v_exp_f32_e32 v129, v74
	ds_read_b64_tr_b16 v[74:75], v230 offset:52224
	ds_read_b64_tr_b16 v[76:77], v230 offset:52736
	s_waitcnt lgkmcnt(8)
	v_mfma_f32_32x32x16_bf16 v[2:17], v[134:137], v[78:81], v[2:17]
	v_sub_f32_e32 v78, v98, v207
	v_exp_f32_e32 v98, v78
	v_sub_f32_e32 v78, v99, v207
	v_exp_f32_e32 v99, v78
	ds_read_b64_tr_b16 v[78:79], v230 offset:56320
	ds_read_b64_tr_b16 v[80:81], v230 offset:56832
	s_waitcnt lgkmcnt(8)
	v_mfma_f32_32x32x16_bf16 v[50:65], v[134:137], v[82:85], v[50:65]
	v_sub_f32_e32 v82, v100, v207
	v_exp_f32_e32 v100, v82
	v_sub_f32_e32 v82, v101, v207
	v_exp_f32_e32 v101, v82
	ds_read_b64_tr_b16 v[82:83], v230 offset:60416
	ds_read_b64_tr_b16 v[84:85], v230 offset:60928
	s_waitcnt lgkmcnt(8)
	v_mfma_f32_32x32x16_bf16 v[34:49], v[134:137], v[86:89], v[34:49]
	v_sub_f32_e32 v86, v102, v207
	v_exp_f32_e32 v102, v86
	v_sub_f32_e32 v86, v103, v207
	v_exp_f32_e32 v103, v86
	ds_read_b64_tr_b16 v[86:87], v230 offset:64512
	ds_read_b64_tr_b16 v[88:89], v230 offset:65024
	s_waitcnt lgkmcnt(8)
	v_mfma_f32_32x32x16_bf16 v[18:33], v[134:137], v[90:93], v[18:33]
	v_sub_f32_e32 v90, v104, v207
	v_exp_f32_e32 v104, v90
	v_sub_f32_e32 v90, v105, v207
	v_exp_f32_e32 v105, v90
	s_waitcnt lgkmcnt(6)
	v_mfma_f32_32x32x16_bf16 v[2:17], v[130:133], v[74:77], v[2:17]
	v_sub_f32_e32 v74, v106, v207
	v_exp_f32_e32 v106, v74
	v_sub_f32_e32 v74, v107, v207
	v_exp_f32_e32 v107, v74
	s_waitcnt lgkmcnt(4)
	v_mfma_f32_32x32x16_bf16 v[50:65], v[130:133], v[78:81], v[50:65]
	v_sub_f32_e32 v74, v108, v207
	v_exp_f32_e32 v108, v74
	v_sub_f32_e32 v74, v109, v207
	v_exp_f32_e32 v109, v74
	s_waitcnt lgkmcnt(2)
	v_mfma_f32_32x32x16_bf16 v[34:49], v[130:133], v[82:85], v[34:49]
	v_sub_f32_e32 v74, v110, v207
	v_exp_f32_e32 v110, v74
	v_sub_f32_e32 v74, v111, v207
	v_exp_f32_e32 v111, v74
	s_waitcnt lgkmcnt(0)
	v_mfma_f32_32x32x16_bf16 v[18:33], v[130:133], v[86:89], v[18:33]
	v_sub_f32_e32 v74, v112, v207
	v_exp_f32_e32 v112, v74
	v_sub_f32_e32 v74, v113, v207
	v_exp_f32_e32 v113, v74
	s_waitcnt vmcnt(4) lgkmcnt(0)
	s_barrier
	s_andn2_b64 vcc, exec, s[4:5]
	s_cbranch_vccnz .LBB0_1031
	v_add_u32_e32 v86, s20, v245
	ds_read_b128 v[74:77], v86 offset:96
	ds_read_b128 v[78:81], v86 offset:64
	ds_read_b128 v[82:85], v86 offset:32
	ds_read_b128 v[86:89], v86
	s_waitcnt lgkmcnt(3)
	v_pk_mul_f32 v[14:15], v[14:15], v[74:75]
	s_waitcnt lgkmcnt(2)
	v_pk_mul_f32 v[10:11], v[10:11], v[78:79]
	s_waitcnt lgkmcnt(1)
	v_pk_mul_f32 v[6:7], v[6:7], v[82:83]
	v_pk_mul_f32 v[16:17], v[16:17], v[76:77]
	v_pk_mul_f32 v[12:13], v[12:13], v[80:81]
	v_pk_mul_f32 v[8:9], v[8:9], v[84:85]
	s_waitcnt lgkmcnt(0)
	v_pk_mul_f32 v[4:5], v[4:5], v[88:89]
	v_pk_mul_f32 v[2:3], v[2:3], v[86:87]
	v_pk_mul_f32 v[62:63], v[62:63], v[74:75]
	v_pk_mul_f32 v[58:59], v[58:59], v[78:79]
	v_pk_mul_f32 v[54:55], v[54:55], v[82:83]
	v_pk_mul_f32 v[64:65], v[64:65], v[76:77]
	v_pk_mul_f32 v[60:61], v[60:61], v[80:81]
	v_pk_mul_f32 v[56:57], v[56:57], v[84:85]
	v_pk_mul_f32 v[52:53], v[52:53], v[88:89]
	v_pk_mul_f32 v[50:51], v[50:51], v[86:87]
	v_pk_mul_f32 v[46:47], v[46:47], v[74:75]
	v_pk_mul_f32 v[42:43], v[42:43], v[78:79]
	v_pk_mul_f32 v[38:39], v[38:39], v[82:83]
	v_pk_mul_f32 v[48:49], v[48:49], v[76:77]
	v_pk_mul_f32 v[44:45], v[44:45], v[80:81]
	v_pk_mul_f32 v[40:41], v[40:41], v[84:85]
	v_pk_mul_f32 v[36:37], v[36:37], v[88:89]
	v_pk_mul_f32 v[34:35], v[34:35], v[86:87]
	v_pk_mul_f32 v[30:31], v[30:31], v[74:75]
	v_pk_mul_f32 v[26:27], v[26:27], v[78:79]
	v_pk_mul_f32 v[22:23], v[22:23], v[82:83]
	v_pk_mul_f32 v[32:33], v[32:33], v[76:77]
	v_pk_mul_f32 v[28:29], v[28:29], v[80:81]
	v_pk_mul_f32 v[24:25], v[24:25], v[84:85]
	v_pk_mul_f32 v[20:21], v[20:21], v[88:89]
	v_pk_mul_f32 v[18:19], v[18:19], v[86:87]
.LBB0_1031:
	s_add_i32 s4, s9, 0x4000
	s_cmpk_lg_u32 s9, 0x8000
	s_cselect_b32 s11, s4, 0
	v_add_u32_e32 v230, s10, v243
	ds_read_b64_tr_b16 v[190:191], v230 offset:49152
	ds_read_b64_tr_b16 v[192:193], v230 offset:49664
	v_mfma_f32_32x32x16_bf16 v[82:97], v[70:73], v[158:161], 0
	v_add_f32_e32 v74, v114, v115
	v_add_f32_e32 v74, v116, v74
	v_add_f32_e32 v74, v117, v74
	v_add_f32_e32 v74, v118, v74
	v_add_f32_e32 v74, v119, v74
	v_cvt_pk_bf16_f32 v150, v114, v115
	v_cvt_pk_bf16_f32 v151, v116, v117
	ds_read_b64_tr_b16 v[186:187], v230 offset:53248
	ds_read_b64_tr_b16 v[188:189], v230 offset:53760
	v_add_f32_e32 v70, v120, v74
	v_add_f32_e32 v70, v121, v70
	v_add_f32_e32 v70, v122, v70
	v_add_f32_e32 v130, v123, v70
	v_mfma_f32_32x32x16_bf16 v[66:81], v[66:69], v[158:161], 0
	v_cvt_pk_bf16_f32 v152, v118, v119
	v_cvt_pk_bf16_f32 v153, v120, v121
	ds_read_b64_tr_b16 v[114:115], v230 offset:57344
	ds_read_b64_tr_b16 v[116:117], v230 offset:57856
	v_mfma_f32_32x32x16_bf16 v[82:97], v[182:185], v[154:157], v[82:97]
	v_add_f32_e32 v118, v124, v130
	v_add_f32_e32 v118, v125, v118
	v_add_f32_e32 v118, v126, v118
	v_add_f32_e32 v130, v127, v118
	v_cvt_pk_bf16_f32 v138, v122, v123
	v_cvt_pk_bf16_f32 v139, v124, v125
	ds_read_b64_tr_b16 v[118:119], v230 offset:61440
	ds_read_b64_tr_b16 v[120:121], v230 offset:61952
	v_mfma_f32_32x32x16_bf16 v[66:81], v[178:181], v[154:157], v[66:81]
	v_add_f32_e32 v122, v128, v130
	v_add_f32_e32 v122, v129, v122
	v_add_f32_e32 v122, v98, v122
	v_add_f32_e32 v130, v99, v122
	v_cvt_pk_bf16_f32 v140, v126, v127
	v_cvt_pk_bf16_f32 v141, v128, v129
	ds_read_b64_tr_b16 v[122:123], v230 offset:50176
	ds_read_b64_tr_b16 v[124:125], v230 offset:50688
	v_mfma_f32_32x32x16_bf16 v[82:97], v[174:177], v[146:149], v[82:97]
	v_add_f32_e32 v126, v100, v130
	v_add_f32_e32 v126, v101, v126
	v_add_f32_e32 v126, v102, v126
	v_add_f32_e32 v130, v103, v126
	v_cvt_pk_bf16_f32 v134, v98, v99
	v_cvt_pk_bf16_f32 v135, v100, v101
	ds_read_b64_tr_b16 v[126:127], v230 offset:54272
	ds_read_b64_tr_b16 v[128:129], v230 offset:54784
	v_mfma_f32_32x32x16_bf16 v[66:81], v[170:173], v[146:149], v[66:81]
	v_add_f32_e32 v98, v104, v130
	v_add_f32_e32 v98, v105, v98
	v_add_f32_e32 v98, v106, v98
	v_add_f32_e32 v98, v107, v98
	v_cvt_pk_bf16_f32 v136, v102, v103
	v_cvt_pk_bf16_f32 v137, v104, v105
	ds_read_b64_tr_b16 v[194:195], v230 offset:58368
	ds_read_b64_tr_b16 v[196:197], v230 offset:58880
	v_mfma_f32_32x32x16_bf16 v[82:97], v[166:169], v[142:145], v[82:97]
	v_add_f32_e32 v98, v108, v98
	v_add_f32_e32 v98, v109, v98
	v_add_f32_e32 v98, v110, v98
	v_add_f32_e32 v98, v111, v98
	v_cvt_pk_bf16_f32 v130, v106, v107
	v_cvt_pk_bf16_f32 v131, v108, v109
	ds_read_b64_tr_b16 v[106:107], v230 offset:62464
	ds_read_b64_tr_b16 v[108:109], v230 offset:62976
	v_mfma_f32_32x32x16_bf16 v[66:81], v[162:165], v[142:145], v[66:81]
	v_add_f32_e32 v98, v112, v98
	v_add_f32_e32 v98, v113, v98
	v_add_f32_e32 v98, 0, v98
	v_cvt_pk_bf16_f32 v132, v110, v111
	v_cvt_pk_bf16_f32 v133, v112, v113
	s_nop 0
	v_add_f32_e32 v234, v234, v98
	s_add_i32 s4, s9, s89
	v_lshl_add_u64 v[98:99], v[220:221], 0, s[0:1]
	s_mov_b32 s5, m0
	s_mov_b32 m0, s4
	s_nop 0
	global_load_lds_dwordx4 v[98:99], off
	s_mov_b32 m0, s5
	v_lshl_add_u64 v[98:99], v[218:219], 0, s[0:1]
	s_addk_i32 s4, 0x400
	s_mov_b32 s5, m0
	s_mov_b32 m0, s4
	s_nop 0
	global_load_lds_dwordx4 v[98:99], off
	s_mov_b32 m0, s5
	v_lshl_add_u64 v[110:111], v[224:225], 0, s[74:75]
	s_add_i32 s4, s11, s70
	s_mov_b32 s5, m0
	s_mov_b32 m0, s4
	s_nop 0
	global_load_lds_dwordx4 v[110:111], off
	s_mov_b32 m0, s5
	v_lshl_add_u64 v[98:99], v[224:225], 0, s[62:63]
	s_addk_i32 s4, 0x400
	s_mov_b32 s5, m0
	s_mov_b32 m0, s4
	s_nop 0
	global_load_lds_dwordx4 v[98:99], off
	s_mov_b32 m0, s5
	s_waitcnt lgkmcnt(14)
	v_mfma_f32_32x32x16_bf16 v[2:17], v[150:153], v[190:193], v[2:17]
	v_max_f32_e32 v98, v83, v83
	v_max_f32_e32 v99, v82, v82
	v_max_f32_e32 v98, v99, v98
	v_max3_f32 v99, v84, v85, v67
	v_max3_f32 v98, v98, v66, v68
	v_max3_f32 v98, v98, v69, v86
	v_max3_f32 v99, v99, v88, v89
	v_max3_f32 v98, v98, v87, v70
	v_max3_f32 v99, v99, v72, v73
	s_waitcnt lgkmcnt(12)
	v_mfma_f32_32x32x16_bf16 v[50:65], v[150:153], v[186:189], v[50:65]
	v_max3_f32 v98, v98, v71, v90
	v_max3_f32 v99, v99, v92, v93
	v_max3_f32 v98, v98, v91, v74
	v_max3_f32 v99, v99, v76, v77
	v_max3_f32 v98, v98, v75, v94
	v_max3_f32 v99, v99, v96, v97
	s_waitcnt lgkmcnt(10)
	v_mfma_f32_32x32x16_bf16 v[34:49], v[150:153], v[114:117], v[34:49]
	v_max3_f32 v98, v98, v95, v78
	v_max3_f32 v99, v99, v80, v81
	v_max3_f32 v98, v98, v79, v99
	v_mov_b32_e32 v99, v98
	s_waitcnt lgkmcnt(8)
	v_mfma_f32_32x32x16_bf16 v[18:33], v[150:153], v[118:121], v[18:33]
	v_permlane32_swap_b32_e32 v98, v99
	v_max_f32_e32 v99, v99, v99
	v_max_f32_e32 v98, v98, v98
	v_max_f32_e32 v98, v98, v99
	v_sub_f32_e32 v98, v98, v207
	v_cmp_lt_f32_e32 vcc, s3, v98
	s_cmp_lg_u64 vcc, 0
	s_cselect_b64 s[4:5], -1, 0
	s_cbranch_vccnz .LBB0_1039
.LBB0_1032:
	s_add_i32 s6, s11, 0
	v_add_u32_e32 v98, s6, v209
	ds_read_b128 v[102:105], v98
	ds_read_b128 v[98:101], v98 offset:8192
	v_sub_f32_e32 v82, v82, v207
	v_sub_f32_e32 v83, v83, v207
	v_exp_f32_e32 v82, v82
	v_exp_f32_e32 v83, v83
	v_add_u32_e32 v112, s6, v213
	ds_read_b128 v[182:185], v112
	ds_read_b128 v[178:181], v112 offset:8192
	v_sub_f32_e32 v84, v84, v207
	v_sub_f32_e32 v85, v85, v207
	v_exp_f32_e32 v84, v84
	v_exp_f32_e32 v85, v85
	v_add_u32_e32 v112, s6, v251
	ds_read_b128 v[174:177], v112
	ds_read_b128 v[170:173], v112 offset:8192
	v_sub_f32_e32 v86, v86, v207
	v_sub_f32_e32 v87, v87, v207
	v_exp_f32_e32 v86, v86
	v_exp_f32_e32 v87, v87
	v_add_u32_e32 v112, s6, v235
	ds_read_b128 v[166:169], v112
	ds_read_b128 v[162:165], v112 offset:8192
	v_sub_f32_e32 v88, v88, v207
	v_sub_f32_e32 v89, v89, v207
	v_exp_f32_e32 v88, v88
	v_exp_f32_e32 v89, v89
	ds_read_b64_tr_b16 v[112:113], v230 offset:51200
	ds_read_b64_tr_b16 v[114:115], v230 offset:51712
	s_waitcnt lgkmcnt(14)
	v_mfma_f32_32x32x16_bf16 v[2:17], v[138:141], v[122:125], v[2:17]
	v_sub_f32_e32 v90, v90, v207
	v_sub_f32_e32 v91, v91, v207
	v_exp_f32_e32 v90, v90
	v_exp_f32_e32 v91, v91
	ds_read_b64_tr_b16 v[116:117], v230 offset:55296
	ds_read_b64_tr_b16 v[118:119], v230 offset:55808
	v_mfma_f32_32x32x16_bf16 v[50:65], v[138:141], v[126:129], v[50:65]
	v_sub_f32_e32 v92, v92, v207
	v_sub_f32_e32 v93, v93, v207
	v_exp_f32_e32 v92, v92
	v_exp_f32_e32 v93, v93
	ds_read_b64_tr_b16 v[120:121], v230 offset:59392
	ds_read_b64_tr_b16 v[122:123], v230 offset:59904
	s_waitcnt lgkmcnt(14)
	v_mfma_f32_32x32x16_bf16 v[34:49], v[138:141], v[194:197], v[34:49]
	v_sub_f32_e32 v94, v94, v207
	v_sub_f32_e32 v95, v95, v207
	v_exp_f32_e32 v94, v94
	v_exp_f32_e32 v95, v95
	ds_read_b64_tr_b16 v[124:125], v230 offset:63488
	ds_read_b64_tr_b16 v[126:127], v230 offset:64000
	v_mfma_f32_32x32x16_bf16 v[18:33], v[138:141], v[106:109], v[18:33]
	v_sub_f32_e32 v96, v96, v207
	v_sub_f32_e32 v97, v97, v207
	v_exp_f32_e32 v96, v96
	v_exp_f32_e32 v97, v97
	ds_read_b64_tr_b16 v[106:107], v230 offset:52224
	ds_read_b64_tr_b16 v[108:109], v230 offset:52736
	s_waitcnt lgkmcnt(8)
	v_mfma_f32_32x32x16_bf16 v[2:17], v[134:137], v[112:115], v[2:17]
	v_sub_f32_e32 v66, v66, v207
	v_sub_f32_e32 v67, v67, v207
	v_exp_f32_e32 v66, v66
	v_exp_f32_e32 v67, v67
	ds_read_b64_tr_b16 v[112:113], v230 offset:56320
	ds_read_b64_tr_b16 v[114:115], v230 offset:56832
	s_waitcnt lgkmcnt(8)
	v_mfma_f32_32x32x16_bf16 v[50:65], v[134:137], v[116:119], v[50:65]
	v_sub_f32_e32 v68, v68, v207
	v_sub_f32_e32 v69, v69, v207
	v_exp_f32_e32 v68, v68
	v_exp_f32_e32 v69, v69
	ds_read_b64_tr_b16 v[116:117], v230 offset:60416
	ds_read_b64_tr_b16 v[118:119], v230 offset:60928
	s_waitcnt lgkmcnt(8)
	v_mfma_f32_32x32x16_bf16 v[34:49], v[134:137], v[120:123], v[34:49]
	v_sub_f32_e32 v70, v70, v207
	v_sub_f32_e32 v71, v71, v207
	v_exp_f32_e32 v70, v70
	v_exp_f32_e32 v71, v71
	ds_read_b64_tr_b16 v[120:121], v230 offset:64512
	ds_read_b64_tr_b16 v[122:123], v230 offset:65024
	s_waitcnt lgkmcnt(8)
	v_mfma_f32_32x32x16_bf16 v[18:33], v[134:137], v[124:127], v[18:33]
	v_sub_f32_e32 v72, v72, v207
	v_sub_f32_e32 v73, v73, v207
	v_exp_f32_e32 v72, v72
	v_exp_f32_e32 v73, v73
	s_waitcnt lgkmcnt(6)
	v_mfma_f32_32x32x16_bf16 v[2:17], v[130:133], v[106:109], v[2:17]
	v_sub_f32_e32 v74, v74, v207
	v_sub_f32_e32 v75, v75, v207
	v_exp_f32_e32 v74, v74
	v_exp_f32_e32 v75, v75
	s_waitcnt lgkmcnt(4)
	v_mfma_f32_32x32x16_bf16 v[50:65], v[130:133], v[112:115], v[50:65]
	v_sub_f32_e32 v76, v76, v207
	v_sub_f32_e32 v77, v77, v207
	v_exp_f32_e32 v76, v76
	v_exp_f32_e32 v77, v77
	s_waitcnt lgkmcnt(2)
	v_mfma_f32_32x32x16_bf16 v[34:49], v[130:133], v[116:119], v[34:49]
	v_sub_f32_e32 v78, v78, v207
	v_sub_f32_e32 v79, v79, v207
	v_exp_f32_e32 v78, v78
	v_exp_f32_e32 v79, v79
	s_waitcnt lgkmcnt(0)
	v_mfma_f32_32x32x16_bf16 v[18:33], v[130:133], v[120:123], v[18:33]
	v_sub_f32_e32 v80, v80, v207
	v_sub_f32_e32 v81, v81, v207
	v_exp_f32_e32 v80, v80
	v_exp_f32_e32 v81, v81
	s_waitcnt vmcnt(4) lgkmcnt(0)
	s_barrier
	s_andn2_b64 vcc, exec, s[4:5]
	s_cbranch_vccnz .LBB0_1034
	v_add_u32_e32 v120, s20, v245
	ds_read_b128 v[106:109], v120 offset:96
	ds_read_b128 v[112:115], v120 offset:64
	ds_read_b128 v[116:119], v120 offset:32
	ds_read_b128 v[120:123], v120
	s_waitcnt lgkmcnt(3)
	v_pk_mul_f32 v[14:15], v[14:15], v[106:107]
	s_waitcnt lgkmcnt(2)
	v_pk_mul_f32 v[10:11], v[10:11], v[112:113]
	s_waitcnt lgkmcnt(1)
	v_pk_mul_f32 v[6:7], v[6:7], v[116:117]
	v_pk_mul_f32 v[16:17], v[16:17], v[108:109]
	v_pk_mul_f32 v[12:13], v[12:13], v[114:115]
	v_pk_mul_f32 v[8:9], v[8:9], v[118:119]
	s_waitcnt lgkmcnt(0)
	v_pk_mul_f32 v[4:5], v[4:5], v[122:123]
	v_pk_mul_f32 v[2:3], v[2:3], v[120:121]
	v_pk_mul_f32 v[62:63], v[62:63], v[106:107]
	v_pk_mul_f32 v[58:59], v[58:59], v[112:113]
	v_pk_mul_f32 v[54:55], v[54:55], v[116:117]
	v_pk_mul_f32 v[64:65], v[64:65], v[108:109]
	v_pk_mul_f32 v[60:61], v[60:61], v[114:115]
	v_pk_mul_f32 v[56:57], v[56:57], v[118:119]
	v_pk_mul_f32 v[52:53], v[52:53], v[122:123]
	v_pk_mul_f32 v[50:51], v[50:51], v[120:121]
	v_pk_mul_f32 v[46:47], v[46:47], v[106:107]
	v_pk_mul_f32 v[42:43], v[42:43], v[112:113]
	v_pk_mul_f32 v[38:39], v[38:39], v[116:117]
	v_pk_mul_f32 v[48:49], v[48:49], v[108:109]
	v_pk_mul_f32 v[44:45], v[44:45], v[114:115]
	v_pk_mul_f32 v[40:41], v[40:41], v[118:119]
	v_pk_mul_f32 v[36:37], v[36:37], v[122:123]
	v_pk_mul_f32 v[34:35], v[34:35], v[120:121]
	v_pk_mul_f32 v[30:31], v[30:31], v[106:107]
	v_pk_mul_f32 v[26:27], v[26:27], v[112:113]
	v_pk_mul_f32 v[22:23], v[22:23], v[116:117]
	v_pk_mul_f32 v[32:33], v[32:33], v[108:109]
	v_pk_mul_f32 v[28:29], v[28:29], v[114:115]
	v_pk_mul_f32 v[24:25], v[24:25], v[118:119]
	v_pk_mul_f32 v[20:21], v[20:21], v[122:123]
	v_pk_mul_f32 v[18:19], v[18:19], v[120:121]
